# attention log-sum-exp scratch addressed head-major [batch][head][token] instead of [token][head] (coalesced 4-byte row accesses, no cross-workgroup line sharing)
# speedup vs baseline: 1.0045x; 1.0045x over previous
; #define LAS __attribute__((address_space(3)))
; #define AT_SU(s_) (2 * AT_P((s_) >> 1) + ((s_) & 1))
; #define AT_FETCH_Q(su_) do { const int su__ = (su_); const bf16* qp_ = QK + ((((size_t)((su__ >> 8) * 16 + ((su__ >> 4) & 15)) << ldil) | ((su__ >> lq4) & dilm)) * Ls + ((su__ & nq4m) * 128 + 16 * wq + n)) * 64 + 8 * kq; \
;         qf[0] = *(const bf16x8s*)qp_; qf[1] = *(const bf16x8s*)(qp_ + 32); } while (0)
; #define AT_SU(s_) (2 * AT_P((s_) >> 1) + ((s_) & 1))
; #define AT_FETCH_Q(su_) do { const int su__ = (su_); const bf16* qp_ = QK + ((((size_t)((su__ >> 8) * 16 + ((su__ >> 4) & 15)) << ldil) | ((su__ >> lq4) & dilm)) * Ls + ((su__ & nq4m) * 128 + 16 * wq + n)) * 64 + 8 * kq; \
;         qf[0] = *(const bf16x8s*)qp_; qf[1] = *(const bf16x8s*)(qp_ + 32); tick += 2; } while (0)
; __device__ __forceinline__ void attn_group_mfma5(const bf16* QK, const float* bias2g, int ldil, int first, bf16* OACC, float* LSE, LAS unsigned char* lds, const int tid, const int bid, const int G) {
;     ...
;         const int su = AT_SU(s), q4 = su & nq4m, rr = (su >> lq4) & dilm, h = (su >> 4) & 15, b = su >> 8;
;         const LAS unsigned char* Kl = lds + (s & 1) * AT5_BUF; const LAS unsigned char* Vl = Kl + 32768; const LAS float* tab = (const LAS float*)(Kl + 65536);
;         const size_t rowq = (size_t)b * SEQ + ((size_t)(q4 * 128 + 16 * wq + n) << ldil) + rr;
;         f32x4 S[9];
; #pragma unroll
;         for (int kb = 0; kb < 9; ++kb) S[kb] = (f32x4){0.f, 0.f, 0.f, 0.f};
;         { const LAS unsigned char* kp0 = Kl + (16 * wq + n) * 128;
; #pragma unroll
;           for (int ks = 0; ks < 2; ++ks)
; #pragma unroll
;             for (int kb = 0; kb < 9; ++kb) S[kb] = __builtin_amdgcn_mfma_f32_16x16x32_bf16(*(const LAS bf16x8s*)(kp0 + 16 * kb * 128 + (((4 * ks + kq) ^ fl) * 16)), qf[ks], S[kb], 0, 0, 0); }
;         __builtin_amdgcn_sched_barrier(0);
;         if (more) AT_FETCH_Q(AT_SU(s + 1));
;         float lold = 0.f; v2u xo[4];
;         if (!first) { lold = LSE[rowq * 16 + h];
; #pragma unroll
;             for (int db = 0; db < 4; ++db) xo[db] = *(const v2u*)(OACC + rowq * D + h * 64 + 16 * db + 4 * kq); }
.LBB0_215:
	s_lshl_b32 s0, s42, 1
	s_or_b32 s0, s0, s36
	s_and_b32 s36, s0, s48
	s_ashr_i32 s8, s42, 7
	s_ashr_i32 s0, s0, s39
	s_ashr_i32 s9, s8, 31
	s_lshl_b32 s36, s36, 7
	s_and_b32 s0, s0, s49
	s_lshl_b64 s[8:9], s[8:9], 11
	v_add_u32_e32 v0, s36, v71
	v_ashrrev_i32_e32 v1, 31, v0
	s_add_u32 s8, s8, s0
	s_addc_u32 s9, s9, 0
	v_lshlrev_b64 v[0:1], s43, v[0:1]
	v_lshl_add_u64 v[0:1], s[8:9], 0, v[0:1]
	v_cndmask_b32_e64 v2, 0, 1, s[44:45]
	v_lshrrev_b32_e32 v52, 11, v0
	v_mul_u32_u24_e32 v52, 0x1e000, v52
	v_lshl_add_u32 v52, v0, 2, v52
	v_mov_b32_e32 v53, 0
	v_lshlrev_b64 v[0:1], 11, v[0:1]
	s_bfe_u32 s0, s42, 0x40003
	v_cmp_ne_u32_e64 s[8:9], 1, v2
	s_andn2_b64 vcc, exec, s[44:45]
	v_lshl_add_u64 v[62:63], s[52:53], 0, v[52:53]
	v_lshl_add_u64 v[60:61], s[46:47], 0, v[0:1]
	v_lshlrev_b32_e32 v58, 1, v50
	s_cbranch_vccnz .LBB0_217
	s_lshl_b32 s60, s0, 13
	v_lshl_add_u64 v[0:1], v[62:63], 0, s[60:61]
	s_lshl_b32 s60, s0, 7
	v_lshl_add_u64 v[52:53], v[60:61], 0, s[60:61]
	v_mov_b32_e32 v59, v3
	v_lshl_add_u64 v[52:53], v[52:53], 0, v[58:59]
	v_lshl_add_u64 v[114:115], v[52:53], 0, v[112:113]
	global_load_dword v59, v[0:1], off
	global_load_dwordx4 v[104:107], v[114:115], off
	global_load_dwordx4 v[108:111], v[114:115], off offset:64
	s_branch .LBB0_218

; __device__ __forceinline__ void attn_group_mfma5(const bf16* QK, const float* bias2g, int ldil, int first, bf16* OACC, float* LSE, LAS unsigned char* lds, const int tid, const int bid, const int G) {
;     ...
;         if (kq == 0) LSE[rowq * 16 + h] = lse;
.LBB0_220:
	s_lshl_b32 s60, s0, 13
	v_lshl_add_u64 v[30:31], v[62:63], 0, s[60:61]
	global_store_dword v[30:31], v28, off

; #define LAS __attribute__((address_space(3)))
; #define AT_SU(s_) (2 * AT_P((s_) >> 1) + ((s_) & 1))
; #define AT_SU(s_) (2 * AT_P((s_) >> 1) + ((s_) & 1))
; __device__ __forceinline__ void attn_group_ring(const bf16* QK, const float* bias2g, int ldil, int first, bf16* OACC, float* LSE, LAS unsigned char* lds, const int tid, const int bid, const int G) {
;     ...
;       AT_FETCH_Q(AT_SU(0)); if (tid < 192) tab[tid] = bv; }
;     int iss = NH < 4 ? NH : 4;
;     AT_WAITH(1);
;     asm volatile("s_waitcnt lgkmcnt(0)" ::: "memory"); __builtin_amdgcn_s_barrier(); asm volatile("" ::: "memory");
;     const int fl = (n >> 1) & 7;
;     for (int s = 0; s < ns; ++s) {
;         const int rn = s / R, jn = s - rn * R, a = rn * RH + jn;
;         if (iss <= a + 3 && iss < NH) { AT_DMAH(iss); ++iss; }
;         if (iss <= a + 3 && iss < NH) { AT_DMAH(iss); ++iss; }
;         const bool more = s + 1 < ns;
;         const int su = AT_SU(s), q4 = su & nq4m, rr = (su >> lq4) & dilm, h = (su >> 4) & 15, b = su >> 8;
;         const size_t rowq = (size_t)b * SEQ + ((size_t)(q4 * 128 + 16 * wq + n) << ldil) + rr;
;         f32x4 S[9];
; #pragma unroll
;         for (int kb = 0; kb < 9; ++kb) S[kb] = (f32x4){0.f, 0.f, 0.f, 0.f};
; #pragma unroll
;         for (int ks = 0; ks < 2; ++ks)
; #pragma unroll
;             for (int kb = 0; kb < 9; ++kb) { const int wrow = 16 * (wq + kb);
;                 const LAS unsigned char* kp = lds + ((a + (wrow >> 7)) & 3) * 32768 + ((wrow & 127) + n) * 128 + (((4 * ks + kq) ^ fl) * 16);
;                 S[kb] = __builtin_amdgcn_mfma_f32_16x16x32_bf16(*(const LAS bf16x8s*)kp, qf[ks], S[kb], 0, 0, 0); }
;         __builtin_amdgcn_sched_barrier(0);
;         if (more) AT_FETCH_Q(AT_SU(s + 1));
;         float lold = 0.f; v2u xo[4];
;         if (!first) { lold = LSE[rowq * 16 + h];
; #pragma unroll
;             for (int db = 0; db < 4; ++db) xo[db] = *(const v2u*)(OACC + rowq * D + h * 64 + 16 * db + 4 * kq); }
;         else {
; #pragma unroll
;             for (int db = 0; db < 4; ++db) xo[db] = (v2u){0u, 0u}; }
;         __builtin_amdgcn_sched_barrier(0);
;         const LAS float* tb = tab + (32 + 4 * kq - n);
;         int kt0 = q4 * 128 - 64 + 16 * wq + 4 * kq; asm volatile("" : "+v"(kt0));
.LBB0_232:
	s_or_b64 exec, exec, s[2:3]
	s_not_b32 s47, s4
	s_not_b32 s48, s5
	s_and_b32 s49, s1, -2
	s_cmp_eq_u32 s24, 0
	s_cselect_b32 s51, 8, 4
	s_cselect_b32 s50, 3, 2
	s_cselect_b32 s1, 1, 2
	s_or_b32 s56, s51, 1
	s_lshl_b32 s57, s56, s1
	s_add_i32 s60, s51, -1
	s_cmp_eq_u32 s24, 1
	v_lshlrev_b32_e32 v12, 2, v51
	s_cselect_b64 s[6:7], -1, 0
	v_sub_u32_e32 v13, v12, v67
	s_add_i32 s1, 0, 0x20000
	v_lshlrev_b32_e32 v2, 3, v51
	v_lshl_add_u32 v65, v13, 2, s1
	s_and_b32 s1, s37, 0x70
	s_waitcnt vmcnt(0)
	v_lshlrev_b32_e32 v0, 1, v2
	v_mov_b32_e32 v1, v3
	v_or_b32_e32 v18, s1, v67
	s_add_i32 s1, s0, 1
	v_lshl_add_u64 v[48:49], s[80:81], 0, v[0:1]
	v_lshrrev_b32_e32 v0, 1, v68
	s_lshl_b32 s4, s1, 4
	v_bitop3_b32 v0, v0, v51, 7 bitop3:0x6c
	s_lshr_b32 s63, s1, 3
	s_and_b32 s1, s4, 0x70
	v_lshlrev_b32_e32 v17, 3, v69
	v_lshlrev_b32_e32 v69, 4, v0
	v_or_b32_e32 v0, s1, v67
	s_add_i32 s1, s0, 2
	s_lshl_b32 s4, s1, 4
	s_lshr_b32 s68, s1, 3
	s_and_b32 s1, s4, 0x70
	v_lshl_add_u32 v71, v0, 7, 0
	v_or_b32_e32 v0, s1, v67
	s_add_i32 s1, s0, 3
	s_lshl_b32 s4, s1, 4
	s_lshr_b32 s72, s1, 3
	s_and_b32 s1, s4, 0x70
	v_lshl_add_u32 v72, v0, 7, 0
	v_or_b32_e32 v0, s1, v67
	s_add_i32 s1, s0, 4
	s_lshl_b32 s4, s1, 4
	s_lshr_b32 s73, s1, 3
	s_and_b32 s1, s4, 0x70
	v_lshl_add_u32 v73, v0, 7, 0
	v_or_b32_e32 v0, s1, v67
	s_add_i32 s1, s0, 5
	s_lshl_b32 s4, s1, 4
	s_lshr_b32 s74, s1, 3
	s_and_b32 s1, s4, 0x70
	v_lshl_add_u32 v74, v0, 7, 0
	v_or_b32_e32 v0, s1, v67
	s_add_i32 s1, s0, 6
	s_lshl_b32 s4, s1, 4
	s_lshr_b32 s75, s1, 3
	s_and_b32 s1, s4, 0x70
	v_lshl_add_u32 v75, v0, 7, 0
	v_or_b32_e32 v0, s1, v67
	s_add_i32 s1, s0, 7
	s_lshl_b32 s4, s1, 4
	s_lshr_b32 s62, s0, 3
	s_lshr_b32 s76, s1, 3
	s_and_b32 s1, s4, 0x70
	s_add_i32 s0, s0, 8
	v_lshl_add_u32 v76, v0, 7, 0
	v_or_b32_e32 v0, s1, v67
	s_lshl_b32 s1, s0, 4
	s_lshr_b32 s77, s0, 3
	s_and_b32 s0, s1, 0x70
	v_lshl_add_u32 v77, v0, 7, 0
	v_or_b32_e32 v0, s0, v67
	s_add_i32 s0, s37, 16
	s_lshr_b32 s79, s0, 7
	s_lshl_b32 s0, s0, 7
	s_and_b32 s5, s0, 0x3800
	s_add_i32 s0, s37, 32
	s_lshr_b32 s82, s0, 7
	s_lshl_b32 s0, s0, 7
	s_and_b32 s10, s0, 0x3800
	s_add_i32 s0, s37, 48
	s_lshr_b32 s83, s0, 7
	s_lshl_b32 s0, s0, 7
	s_and_b32 s11, s0, 0x3800
	s_add_i32 s0, s37, 64
	s_lshr_b32 s84, s0, 7
	s_lshl_b32 s0, s0, 7
	s_and_b32 s38, s0, 0x3800
	s_add_i32 s0, s37, 0x50
	s_lshr_b32 s85, s0, 7
	s_lshl_b32 s0, s0, 7
	s_and_b32 s40, s0, 0x3800
	s_add_i32 s0, s37, 0x60
	s_lshr_b32 s86, s0, 7
	s_lshl_b32 s0, s0, 7
	s_and_b32 s41, s0, 0x3800
	s_add_i32 s0, s37, 0x70
	s_lshr_b32 s89, s0, 7
	s_lshl_b32 s0, s0, 7
	s_and_b32 s42, s0, 0x3800
	s_add_i32 s0, s37, 0x80
	v_lshrrev_b32_e32 v16, 2, v67
	s_lshr_b32 s78, s37, 7
	s_and_b32 s4, s36, 0x3800
	s_lshr_b32 s91, s0, 7
	s_lshl_b32 s0, s46, 13
	v_bfe_u32 v1, v68, 1, 3
	v_lshlrev_b32_e32 v13, 2, v66
	v_or_b32_e32 v16, v12, v16
	v_and_b32_e32 v17, 8, v17
	s_add_u32 s0, s96, s0
	v_or_b32_e32 v64, s37, v67
	v_xor_b32_e32 v70, 0x80, v13
	v_lshlrev_b32_e32 v13, 1, v51
	v_lshrrev_b32_e32 v14, 3, v67
	v_lshl_or_b32 v16, v16, 7, v17
	v_bfe_u32 v17, v68, 1, 1
	v_lshl_add_u32 v67, v0, 7, 0
	v_bitop3_b32 v0, v51, v1, 4 bitop3:0x36
	s_addc_u32 s1, s97, 0
	v_or_b32_e32 v15, v13, v14
	v_lshlrev_b32_e32 v78, 4, v0
	v_bitop3_b32 v0, v13, v17, v14 bitop3:0x36
	s_add_u32 s8, s0, 0x21a00000
	v_lshl_or_b32 v79, v0, 4, v16
	v_bitop3_b32 v0, v17, v15, 2 bitop3:0x36
	s_addc_u32 s9, s1, 0
	s_lshl_b32 s0, s46, 7
	v_lshl_or_b32 v80, v0, 4, v16
	v_bitop3_b32 v0, v17, v15, 4 bitop3:0x36
	s_add_u32 s0, s96, s0
	v_lshl_or_b32 v81, v0, 4, v16
	v_bitop3_b32 v0, v17, v15, 6 bitop3:0x36
	s_addc_u32 s1, s97, 0
	v_lshl_or_b32 v82, v0, 4, v16
	v_lshl_add_u64 v[0:1], s[0:1], 0, v[2:3]
	s_mov_b64 s[0:1], 0x1da00000
	v_lshl_add_u64 v[50:51], v[0:1], 0, s[0:1]
	v_add_u32_e32 v0, s37, v12
	v_subrev_u32_e32 v83, 64, v0
	v_cvt_f32_ubyte0_e32 v0, s56
	v_rcp_iflag_f32_e32 v0, v0
	s_waitcnt vmcnt(8)
	s_sub_i32 s0, 0, s56
	s_mov_b32 s53, s17
	v_mul_f32_e32 v0, 0x4f7ffffe, v0
	v_cvt_u32_f32_e32 v0, v0
	s_mov_b32 s52, 4
	s_waitcnt lgkmcnt(0)
	s_barrier
	v_readfirstlane_b32 s1, v0
	s_mul_i32 s0, s0, s1
	s_mov_b64 s[54:55], s[18:19]
	s_mul_hi_u32 s0, s1, s0
	s_mov_b64 s[16:17], s[52:53]
	s_mov_b32 s87, 0
	v_writelane_b32 v255, s24, 5
	v_cmp_gt_u32_e64 s[2:3], 16, v66
	v_lshl_add_u32 v68, v18, 7, 0
	s_mov_b64 s[24:25], s[96:97]
	s_add_i32 s92, s1, s0
	s_add_i32 s93, s4, 0
	s_add_i32 s95, s5, 0
	s_add_i32 s96, s10, 0
	s_add_i32 s97, s11, 0
	s_add_i32 s58, s38, 0
	s_add_i32 s59, s40, 0
	s_add_i32 s38, s41, 0
	s_add_i32 s40, s42, 0
	s_mov_b32 s41, 18
	s_mov_b64 s[18:19], s[54:55]
	s_branch .LBB0_234

; #define LAS __attribute__((address_space(3)))
; #define AT_SU(s_) (2 * AT_P((s_) >> 1) + ((s_) & 1))
; #define AT_FETCH_Q(su_) do { const int su__ = (su_); const bf16* qp_ = QK + ((((size_t)((su__ >> 8) * 16 + ((su__ >> 4) & 15)) << ldil) | ((su__ >> lq4) & dilm)) * Ls + ((su__ & nq4m) * 128 + 16 * wq + n)) * 64 + 8 * kq; \
;         qf[0] = *(const bf16x8s*)qp_; qf[1] = *(const bf16x8s*)(qp_ + 32); } while (0)
; #define AT_SU(s_) (2 * AT_P((s_) >> 1) + ((s_) & 1))
; #define AT_FETCH_Q(su_) do { const int su__ = (su_); const bf16* qp_ = QK + ((((size_t)((su__ >> 8) * 16 + ((su__ >> 4) & 15)) << ldil) | ((su__ >> lq4) & dilm)) * Ls + ((su__ & nq4m) * 128 + 16 * wq + n)) * 64 + 8 * kq; \
;         qf[0] = *(const bf16x8s*)qp_; qf[1] = *(const bf16x8s*)(qp_ + 32); tick += 2; } while (0)
; __device__ __forceinline__ void attn_group_ring(const bf16* QK, const float* bias2g, int ldil, int first, bf16* OACC, float* LSE, LAS unsigned char* lds, const int tid, const int bid, const int G) {
;     ...
;         const int su = AT_SU(s), q4 = su & nq4m, rr = (su >> lq4) & dilm, h = (su >> 4) & 15, b = su >> 8;
;         const size_t rowq = (size_t)b * SEQ + ((size_t)(q4 * 128 + 16 * wq + n) << ldil) + rr;
;         f32x4 S[9];
; #pragma unroll
;         for (int kb = 0; kb < 9; ++kb) S[kb] = (f32x4){0.f, 0.f, 0.f, 0.f};
; #pragma unroll
;         for (int ks = 0; ks < 2; ++ks)
; #pragma unroll
;             for (int kb = 0; kb < 9; ++kb) { const int wrow = 16 * (wq + kb);
;                 const LAS unsigned char* kp = lds + ((a + (wrow >> 7)) & 3) * 32768 + ((wrow & 127) + n) * 128 + (((4 * ks + kq) ^ fl) * 16);
;                 S[kb] = __builtin_amdgcn_mfma_f32_16x16x32_bf16(*(const LAS bf16x8s*)kp, qf[ks], S[kb], 0, 0, 0); }
;         __builtin_amdgcn_sched_barrier(0);
;         if (more) AT_FETCH_Q(AT_SU(s + 1));
;         float lold = 0.f; v2u xo[4];
;         if (!first) { lold = LSE[rowq * 16 + h];
; #pragma unroll
;             for (int db = 0; db < 4; ++db) xo[db] = *(const v2u*)(OACC + rowq * D + h * 64 + 16 * db + 4 * kq); }
.LBB0_240:
	s_bfe_u32 s1, s87, 0x20001
	s_cmp_lt_u32 s87, 8
	s_cselect_b64 s[4:5], -1, 0
	v_cndmask_b32_e64 v0, 0, 1, s[4:5]
	v_cndmask_b32_e64 v2, 0, 1, s[6:7]
	v_readfirstlane_b32 s4, v0
	s_or_b32 s4, s49, s4
	s_lshl_b32 s5, s4, 7
	s_or_b32 s1, s5, s1
	s_or_b32 s1, s1, s45
	s_lshl_b32 s1, s1, 1
	s_and_b32 s5, s87, 1
	s_or_b32 s1, s1, s5
	s_and_b32 s70, s1, s47
	s_ashr_i32 s1, s1, s14
	s_and_b32 s71, s1, s48
	s_lshl_b32 s1, s70, 7
	s_ashr_i32 s5, s4, 31
	v_add_u32_e32 v0, s1, v64
	s_lshl_b64 s[4:5], s[4:5], 11
	v_ashrrev_i32_e32 v1, 31, v0
	s_or_b32 s4, s4, s71
	v_lshlrev_b64 v[0:1], s43, v[0:1]
	v_lshl_add_u64 v[0:1], s[4:5], 0, v[0:1]
	v_lshrrev_b32_e32 v52, 11, v0
	v_mul_u32_u24_e32 v52, 0x1e000, v52
	v_lshl_add_u32 v52, v0, 2, v52
	v_mov_b32_e32 v53, 0
	v_lshlrev_b64 v[0:1], 11, v[0:1]
	v_cmp_ne_u32_e64 s[4:5], 1, v2
	s_andn2_b64 vcc, exec, s[6:7]
	v_lshl_add_u64 v[60:61], s[8:9], 0, v[52:53]
	v_lshl_add_u64 v[52:53], v[50:51], 0, v[0:1]
	v_lshl_add_u64 v[114:115], v[52:53], 0, v[112:113]
	s_cbranch_vccnz .LBB0_242
	global_load_dword v84, v[60:61], off
	global_load_dwordx4 v[104:107], v[114:115], off
	global_load_dwordx4 v[108:111], v[114:115], off offset:64
	s_branch .LBB0_243
